# attention softmax: cross-half (permlane32) combine of row max only in the rare rescale path, row-sum halves combined once per q-block instead of per tile, on top of v28
# speedup vs baseline: 1.0042x; 1.0042x over previous
.LBB0_809:
	s_nop 7
	v_max_f32_e32 v175, v82, v83


	v_max3_f32 v175, v175, v84, v85
	v_max3_f32 v175, v175, v86, v87
	v_max3_f32 v175, v175, v88, v89
	v_max3_f32 v175, v175, v90, v91
	v_max3_f32 v175, v175, v92, v93
	v_max3_f32 v175, v175, v94, v95
	v_max3_f32 v175, v175, v96, v97
	v_max3_f32 v175, v175, v66, v67
	v_max3_f32 v175, v175, v68, v69
	v_max3_f32 v175, v175, v70, v71
	v_max3_f32 v175, v175, v72, v73
	v_max3_f32 v175, v175, v74, v75
	v_max3_f32 v175, v175, v76, v77
	v_max3_f32 v175, v175, v78, v79
	v_max3_f32 v175, v175, v80, v81
	v_cmp_ge_f32_e32 vcc, s76, v175
	s_cmp_eq_u64 vcc, exec
	s_cbranch_scc0 .Lsm1_slow
	v_mov_b32_e32 v222, 1.0
.Lsm1_join:
	v_exp_f32_e32 v82, v82
	v_exp_f32_e32 v66, v66
	v_exp_f32_e32 v175, v83
	v_exp_f32_e32 v67, v67
	v_exp_f32_e32 v84, v84
	v_exp_f32_e32 v68, v68
	v_exp_f32_e32 v85, v85
	v_exp_f32_e32 v69, v69
	v_add_f32_e32 v83, v66, v82
	v_exp_f32_e32 v86, v86
	v_exp_f32_e32 v70, v70
	v_add_f32_e32 v83, 0, v83
	v_add_f32_e32 v176, v67, v175
	v_add_f32_e32 v83, v176, v83
	v_add_f32_e32 v176, v68, v84
	v_add_f32_e32 v83, v176, v83
	v_add_f32_e32 v176, v69, v85
	v_add_f32_e32 v83, v176, v83
	v_add_f32_e32 v176, v70, v86
	v_exp_f32_e32 v87, v87
	v_exp_f32_e32 v71, v71
	v_add_f32_e32 v178, v176, v83
	v_exp_f32_e32 v88, v88
	v_exp_f32_e32 v72, v72
	v_add_f32_e32 v179, v71, v87
	v_exp_f32_e32 v176, v89
	v_exp_f32_e32 v83, v73
	v_add_f32_e32 v73, v179, v178
	v_add_f32_e32 v89, v72, v88
	v_add_f32_e32 v178, v89, v73
	v_exp_f32_e32 v89, v90
	v_exp_f32_e32 v73, v74
	v_add_f32_e32 v179, v83, v176
	v_exp_f32_e32 v90, v91
	v_mov_b32_e32 v74, v75
	v_add_f32_e32 v75, v179, v178
	v_add_f32_e32 v91, v73, v89
	v_add_f32_e32 v178, v91, v75
	v_exp_f32_e32 v74, v74
	v_exp_f32_e32 v91, v92
	v_exp_f32_e32 v75, v76
	v_add_f32_e32 v179, v74, v90
	v_exp_f32_e32 v92, v93
	v_mov_b32_e32 v76, v77
	v_add_f32_e32 v77, v179, v178
	v_add_f32_e32 v93, v75, v91
	v_add_f32_e32 v178, v93, v77
	v_exp_f32_e32 v76, v76
	v_exp_f32_e32 v93, v94
	v_exp_f32_e32 v77, v78
	v_add_f32_e32 v179, v76, v92
	v_exp_f32_e32 v94, v95
	v_mov_b32_e32 v78, v79
	v_add_f32_e32 v79, v179, v178
	v_add_f32_e32 v95, v77, v93
	v_exp_f32_e32 v78, v78
	v_add_f32_e32 v79, v95, v79
	v_exp_f32_e32 v95, v96
	v_exp_f32_e32 v80, v80
	v_exp_f32_e32 v96, v97
	v_exp_f32_e32 v81, v81
	v_add_f32_e32 v178, v78, v94
	v_add_f32_e32 v79, v178, v79
	v_add_f32_e32 v97, v80, v95
	v_add_f32_e32 v79, v97, v79
	v_add_f32_e32 v97, v81, v96
	v_add_f32_e32 v79, v97, v79
	v_mov_b32_e32 v97, v222
	v_cmp_gt_f32_e32 vcc, 1.0, v97


	s_cbranch_vccz .LBB0_813
	s_and_saveexec_b64 s[56:57], s[0:1]
	ds_write_b32 v160, v97
	s_or_b64 exec, exec, s[56:57]
	s_waitcnt lgkmcnt(0)
	v_add_u32_e32 v190, s65, v148
	ds_read_b128 v[178:181], v190 offset:96
	ds_read_b128 v[182:185], v190 offset:64
	ds_read_b128 v[186:189], v190 offset:32
	ds_read_b128 v[190:193], v190
	s_waitcnt lgkmcnt(0)
	v_pk_mul_f32 v[62:63], v[62:63], v[178:179]
	v_pk_mul_f32 v[58:59], v[58:59], v[182:183]
	v_pk_mul_f32 v[54:55], v[54:55], v[186:187]
	v_pk_mul_f32 v[64:65], v[64:65], v[180:181]
	v_pk_mul_f32 v[60:61], v[60:61], v[184:185]
	v_pk_mul_f32 v[56:57], v[56:57], v[188:189]
	v_pk_mul_f32 v[52:53], v[52:53], v[192:193]
	v_pk_mul_f32 v[50:51], v[50:51], v[190:191]
	v_pk_mul_f32 v[46:47], v[46:47], v[178:179]
	v_pk_mul_f32 v[42:43], v[42:43], v[182:183]
	v_pk_mul_f32 v[38:39], v[38:39], v[186:187]
	v_pk_mul_f32 v[48:49], v[48:49], v[180:181]
	v_pk_mul_f32 v[44:45], v[44:45], v[184:185]
	v_pk_mul_f32 v[40:41], v[40:41], v[188:189]
	v_pk_mul_f32 v[36:37], v[36:37], v[192:193]
	v_pk_mul_f32 v[34:35], v[34:35], v[190:191]
	v_pk_mul_f32 v[30:31], v[30:31], v[178:179]
	v_pk_mul_f32 v[26:27], v[26:27], v[182:183]
	v_pk_mul_f32 v[22:23], v[22:23], v[186:187]
	v_pk_mul_f32 v[32:33], v[32:33], v[180:181]
	v_pk_mul_f32 v[28:29], v[28:29], v[184:185]
	v_pk_mul_f32 v[24:25], v[24:25], v[188:189]
	v_pk_mul_f32 v[20:21], v[20:21], v[192:193]
	v_pk_mul_f32 v[18:19], v[18:19], v[190:191]
	v_pk_mul_f32 v[14:15], v[14:15], v[178:179]
	v_pk_mul_f32 v[10:11], v[10:11], v[182:183]
	v_pk_mul_f32 v[6:7], v[6:7], v[186:187]
	v_pk_mul_f32 v[16:17], v[16:17], v[180:181]
	v_pk_mul_f32 v[12:13], v[12:13], v[184:185]
	v_pk_mul_f32 v[8:9], v[8:9], v[188:189]
	v_pk_mul_f32 v[4:5], v[4:5], v[192:193]
	v_pk_mul_f32 v[2:3], v[2:3], v[190:191]
.LBB0_813:
	v_cvt_pk_bf16_f32 v178, v82, v175
	v_cvt_pk_bf16_f32 v179, v84, v85
	v_cvt_pk_bf16_f32 v180, v86, v87
	v_cvt_pk_bf16_f32 v181, v88, v176
	v_cvt_pk_bf16_f32 v84, v89, v90
	v_cvt_pk_bf16_f32 v85, v91, v92
	v_cvt_pk_bf16_f32 v86, v93, v94
	v_cvt_pk_bf16_f32 v87, v95, v96
	v_cvt_pk_bf16_f32 v66, v66, v67
	v_cvt_pk_bf16_f32 v67, v68, v69
	v_cvt_pk_bf16_f32 v68, v70, v71
	v_cvt_pk_bf16_f32 v69, v72, v83
	v_cvt_pk_bf16_f32 v70, v73, v74
	v_cvt_pk_bf16_f32 v71, v75, v76
	v_cvt_pk_bf16_f32 v72, v77, v78
	v_cvt_pk_bf16_f32 v73, v80, v81
	v_lshl_add_u32 v78, s87, 14, v172
	ds_read_b64_tr_b16 v[74:75], v78 offset:0
	ds_read_b64_tr_b16 v[76:77], v78 offset:0x800
	ds_read_b64_tr_b16 v[80:81], v78 offset:0x1000
	ds_read_b64_tr_b16 v[82:83], v78 offset:0x1800
	ds_read_b64_tr_b16 v[88:89], v78 offset:0x2000
	ds_read_b64_tr_b16 v[90:91], v78 offset:0x2800
	ds_read_b64_tr_b16 v[92:93], v78 offset:0x3000

	ds_read_b64_tr_b16 v[94:95], v78 offset:0x3800
	v_fmac_f32_e32 v79, v174, v97
	ds_read_b64_tr_b16 v[174:175], v78 offset:0x200
	ds_read_b64_tr_b16 v[176:177], v78 offset:0xa00
	ds_read_b64_tr_b16 v[182:183], v78 offset:0x1200
	ds_read_b64_tr_b16 v[184:185], v78 offset:0x1a00
	ds_read_b64_tr_b16 v[186:187], v78 offset:0x2200
	ds_read_b64_tr_b16 v[188:189], v78 offset:0x2a00
	ds_read_b64_tr_b16 v[190:191], v78 offset:0x3200
	ds_read_b64_tr_b16 v[192:193], v78 offset:0x3a00
	s_waitcnt lgkmcnt(8)


	v_mfma_f32_32x32x16_bf16 v[50:65], v[178:181], v[74:77], v[50:65]
	ds_read_b64_tr_b16 v[74:75], v78 offset:0x400
	ds_read_b64_tr_b16 v[76:77], v78 offset:0xc00
	v_mfma_f32_32x32x16_bf16 v[50:65], v[84:87], v[80:83], v[50:65]
	ds_read_b64_tr_b16 v[80:81], v78 offset:0x1400
	ds_read_b64_tr_b16 v[82:83], v78 offset:0x1c00
	v_mfma_f32_32x32x16_bf16 v[50:65], v[66:69], v[88:91], v[50:65]
	ds_read_b64_tr_b16 v[88:89], v78 offset:0x2400
	ds_read_b64_tr_b16 v[90:91], v78 offset:0x2c00
	v_mfma_f32_32x32x16_bf16 v[50:65], v[70:73], v[92:95], v[50:65]
	ds_read_b64_tr_b16 v[92:93], v78 offset:0x3400
	ds_read_b64_tr_b16 v[94:95], v78 offset:0x3c00
	s_waitcnt lgkmcnt(8)
	v_mfma_f32_32x32x16_bf16 v[34:49], v[178:181], v[174:177], v[34:49]
	ds_read_b64_tr_b16 v[174:175], v78 offset:0x600
	ds_read_b64_tr_b16 v[176:177], v78 offset:0xe00
	v_mfma_f32_32x32x16_bf16 v[34:49], v[84:87], v[182:185], v[34:49]
	ds_read_b64_tr_b16 v[182:183], v78 offset:0x1600
	ds_read_b64_tr_b16 v[184:185], v78 offset:0x1e00
	v_mfma_f32_32x32x16_bf16 v[34:49], v[66:69], v[186:189], v[34:49]
	ds_read_b64_tr_b16 v[186:187], v78 offset:0x2600
	ds_read_b64_tr_b16 v[188:189], v78 offset:0x2e00
	v_mfma_f32_32x32x16_bf16 v[34:49], v[70:73], v[190:193], v[34:49]
	ds_read_b64_tr_b16 v[190:191], v78 offset:0x3600
	ds_read_b64_tr_b16 v[192:193], v78 offset:0x3e00
	s_waitcnt lgkmcnt(8)
	v_mfma_f32_32x32x16_bf16 v[18:33], v[178:181], v[74:77], v[18:33]
	s_waitcnt lgkmcnt(0)
	v_mfma_f32_32x32x16_bf16 v[18:33], v[84:87], v[80:83], v[18:33]
	v_mfma_f32_32x32x16_bf16 v[18:33], v[66:69], v[88:91], v[18:33]
	v_mfma_f32_32x32x16_bf16 v[18:33], v[70:73], v[92:95], v[18:33]
	v_mfma_f32_32x32x16_bf16 v[2:17], v[178:181], v[174:177], v[2:17]
	s_add_i32 s86, s86, 64
	s_add_i32 s12, s12, 1
	s_add_u32 s94, s94, s16
	s_addc_u32 s95, s95, s17
	s_add_u32 s96, s96, s14
	s_addc_u32 s97, s97, s15


	v_mfma_f32_32x32x16_bf16 v[2:17], v[84:87], v[182:185], v[2:17]
	v_subrev_u32_e32 v168, 64, v168
	s_cmp_eq_u32 s83, s86
	v_mfma_f32_32x32x16_bf16 v[2:17], v[66:69], v[186:189], v[2:17]
	v_mfma_f32_32x32x16_bf16 v[2:17], v[70:73], v[190:193], v[2:17]
	s_cbranch_scc1 .LBB0_815
	v_mov_b32_e32 v174, v79
	s_add_i32 s56, s86, 0xe0
	s_cmp_ge_i32 s56, s84
	s_cbranch_scc0 .LBB0_805

.Lsm1_slow:
	v_mov_b32_e32 v176, v175
	s_nop 1
	v_permlane32_swap_b32_e32 v175, v176
	v_max_f32_e32 v175, v175, v176
	v_max_f32_e32 v175, 0, v175
	v_sub_f32_e32 v66, v66, v175
	v_sub_f32_e32 v67, v67, v175
	v_sub_f32_e32 v68, v68, v175
	v_sub_f32_e32 v69, v69, v175
	v_sub_f32_e32 v70, v70, v175
	v_sub_f32_e32 v71, v71, v175
	v_sub_f32_e32 v72, v72, v175
	v_sub_f32_e32 v73, v73, v175
	v_sub_f32_e32 v74, v74, v175
	v_sub_f32_e32 v75, v75, v175
	v_sub_f32_e32 v76, v76, v175
	v_sub_f32_e32 v77, v77, v175
	v_sub_f32_e32 v78, v78, v175
	v_sub_f32_e32 v79, v79, v175
	v_sub_f32_e32 v80, v80, v175
	v_sub_f32_e32 v81, v81, v175
	v_sub_f32_e32 v82, v82, v175
	v_sub_f32_e32 v83, v83, v175
	v_sub_f32_e32 v84, v84, v175
	v_sub_f32_e32 v85, v85, v175
	v_sub_f32_e32 v86, v86, v175
	v_sub_f32_e32 v87, v87, v175
	v_sub_f32_e32 v88, v88, v175
	v_sub_f32_e32 v89, v89, v175
	v_sub_f32_e32 v90, v90, v175
	v_sub_f32_e32 v91, v91, v175
	v_sub_f32_e32 v92, v92, v175
	v_sub_f32_e32 v93, v93, v175
	v_sub_f32_e32 v94, v94, v175
	v_sub_f32_e32 v95, v95, v175
	v_sub_f32_e32 v96, v96, v175
	v_sub_f32_e32 v97, v97, v175
	v_exp_f32_e64 v222, -v175
	v_add_f32_e32 v173, v173, v175
	v_sub_f32_e32 v206, 0, v173
	v_mov_b32_e32 v207, v206
	v_mov_b32_e32 v208, v206
	v_mov_b32_e32 v209, v206
	v_mov_b32_e32 v210, v206
	v_mov_b32_e32 v211, v206
	v_mov_b32_e32 v212, v206
	v_mov_b32_e32 v213, v206
	v_mov_b32_e32 v214, v206
	v_mov_b32_e32 v215, v206
	v_mov_b32_e32 v216, v206
	v_mov_b32_e32 v217, v206
	v_mov_b32_e32 v218, v206
	v_mov_b32_e32 v219, v206
	v_mov_b32_e32 v220, v206
	v_mov_b32_e32 v221, v206
	s_branch .Lsm1_join
.LBB0_815:
	v_mov_b32_e32 v177, v79
	s_nop 1
	v_permlane32_swap_b32_e32 v79, v177
	v_add_f32_e32 v79, v79, v177
	s_and_saveexec_b64 s[56:57], s[0:1]
	s_cbranch_execz .LBB0_817
	v_div_scale_f32 v66, s[0:1], v79, v79, 1.0
	v_rcp_f32_e32 v67, v66
	v_div_scale_f32 v68, vcc, 1.0, v79, 1.0
	v_fma_f32 v69, -v66, v67, 1.0
	v_fmac_f32_e32 v67, v69, v67
	v_mul_f32_e32 v69, v68, v67
	v_fma_f32 v70, -v66, v69, v68
	v_fmac_f32_e32 v69, v70, v67
	v_fma_f32 v66, -v66, v69, v68
	v_div_fmas_f32 v66, v66, v67, v69
	v_div_fixup_f32 v66, v66, v79, 1.0
	ds_write_b32 v160, v66 offset:128

.LBB0_950:
	s_nop 7
	v_max_f32_e32 v177, v66, v67


	v_max3_f32 v177, v177, v68, v69
	v_max3_f32 v177, v177, v70, v71
	v_max3_f32 v177, v177, v72, v73
	v_max3_f32 v177, v177, v74, v75
	v_max3_f32 v177, v177, v76, v77
	v_max3_f32 v177, v177, v78, v79
	v_max3_f32 v177, v177, v80, v81
	v_max3_f32 v177, v177, v82, v83
	v_max3_f32 v177, v177, v84, v85
	v_max3_f32 v177, v177, v86, v87
	v_max3_f32 v177, v177, v88, v89
	v_max3_f32 v177, v177, v90, v91
	v_max3_f32 v177, v177, v92, v93
	v_max3_f32 v177, v177, v94, v95
	v_max3_f32 v177, v177, v96, v97
	v_cmp_ge_f32_e32 vcc, s76, v177
	s_cmp_eq_u64 vcc, exec
	s_cbranch_scc0 .Lsm2_slow
	v_mov_b32_e32 v226, 1.0
.Lsm2_join:
	v_exp_f32_e32 v177, v66
	v_exp_f32_e32 v66, v82
	v_exp_f32_e32 v178, v67
	v_exp_f32_e32 v67, v83
	v_exp_f32_e32 v83, v68
	v_exp_f32_e32 v68, v84
	v_add_f32_e32 v82, v66, v177
	v_add_f32_e32 v82, 0, v82
	v_add_f32_e32 v179, v67, v178
	v_exp_f32_e32 v84, v69
	v_add_f32_e32 v82, v179, v82
	v_mov_b32_e32 v69, v85
	v_add_f32_e32 v85, v68, v83
	v_exp_f32_e32 v69, v69
	v_add_f32_e32 v82, v85, v82
	v_exp_f32_e32 v85, v70
	v_exp_f32_e32 v70, v86
	v_add_f32_e32 v179, v69, v84
	v_exp_f32_e32 v86, v71
	v_add_f32_e32 v82, v179, v82
	v_mov_b32_e32 v71, v87
	v_add_f32_e32 v87, v70, v85
	v_exp_f32_e32 v71, v71
	v_add_f32_e32 v181, v87, v82
	v_exp_f32_e32 v87, v72
	v_exp_f32_e32 v72, v88
	v_add_f32_e32 v182, v71, v86
	v_exp_f32_e32 v179, v73
	v_exp_f32_e32 v82, v89
	v_add_f32_e32 v73, v182, v181
	v_add_f32_e32 v88, v72, v87
	v_add_f32_e32 v181, v88, v73
	v_exp_f32_e32 v88, v74
	v_exp_f32_e32 v73, v90
	v_add_f32_e32 v182, v82, v179
	v_mov_b32_e32 v74, v75
	v_add_f32_e32 v75, v182, v181
	v_add_f32_e32 v90, v73, v88
	v_exp_f32_e32 v89, v74
	v_add_f32_e32 v181, v90, v75
	v_exp_f32_e32 v74, v91
	v_exp_f32_e32 v90, v76
	v_exp_f32_e32 v75, v92
	v_add_f32_e32 v182, v74, v89
	v_mov_b32_e32 v76, v77
	v_add_f32_e32 v77, v182, v181
	v_add_f32_e32 v92, v75, v90
	v_exp_f32_e32 v91, v76
	v_add_f32_e32 v181, v92, v77
	v_exp_f32_e32 v76, v93
	v_exp_f32_e32 v92, v78
	v_exp_f32_e32 v77, v94
	v_add_f32_e32 v182, v76, v91
	v_mov_b32_e32 v78, v79
	v_add_f32_e32 v79, v182, v181
	v_add_f32_e32 v94, v77, v92
	v_exp_f32_e32 v93, v78
	v_add_f32_e32 v181, v94, v79
	v_exp_f32_e32 v78, v95
	v_exp_f32_e32 v94, v80
	v_exp_f32_e32 v79, v96
	v_exp_f32_e32 v95, v81
	v_exp_f32_e32 v80, v97
	v_add_f32_e32 v182, v78, v93
	v_add_f32_e32 v81, v182, v181
	v_add_f32_e32 v96, v79, v94
	v_add_f32_e32 v81, v96, v81
	v_add_f32_e32 v96, v80, v95
	v_add_f32_e32 v81, v96, v81
	v_mov_b32_e32 v96, v226
	v_cmp_gt_f32_e32 vcc, 1.0, v96


	s_cbranch_vccz .LBB0_954
	s_and_saveexec_b64 s[44:45], s[0:1]
	ds_write_b32 v168, v96
	s_or_b64 exec, exec, s[44:45]
	s_waitcnt lgkmcnt(0)
	v_add_u32_e32 v192, s65, v148
	ds_read_b128 v[180:183], v192 offset:96
	ds_read_b128 v[184:187], v192 offset:64
	ds_read_b128 v[188:191], v192 offset:32
	ds_read_b128 v[192:195], v192
	s_waitcnt lgkmcnt(0)
	v_pk_mul_f32 v[62:63], v[62:63], v[180:181]
	v_pk_mul_f32 v[58:59], v[58:59], v[184:185]
	v_pk_mul_f32 v[54:55], v[54:55], v[188:189]
	v_pk_mul_f32 v[64:65], v[64:65], v[182:183]
	v_pk_mul_f32 v[60:61], v[60:61], v[186:187]
	v_pk_mul_f32 v[56:57], v[56:57], v[190:191]
	v_pk_mul_f32 v[52:53], v[52:53], v[194:195]
	v_pk_mul_f32 v[50:51], v[50:51], v[192:193]
	v_pk_mul_f32 v[46:47], v[46:47], v[180:181]
	v_pk_mul_f32 v[42:43], v[42:43], v[184:185]
	v_pk_mul_f32 v[38:39], v[38:39], v[188:189]
	v_pk_mul_f32 v[48:49], v[48:49], v[182:183]
	v_pk_mul_f32 v[44:45], v[44:45], v[186:187]
	v_pk_mul_f32 v[40:41], v[40:41], v[190:191]
	v_pk_mul_f32 v[36:37], v[36:37], v[194:195]
	v_pk_mul_f32 v[34:35], v[34:35], v[192:193]
	v_pk_mul_f32 v[30:31], v[30:31], v[180:181]
	v_pk_mul_f32 v[26:27], v[26:27], v[184:185]
	v_pk_mul_f32 v[22:23], v[22:23], v[188:189]
	v_pk_mul_f32 v[32:33], v[32:33], v[182:183]
	v_pk_mul_f32 v[28:29], v[28:29], v[186:187]
	v_pk_mul_f32 v[24:25], v[24:25], v[190:191]
	v_pk_mul_f32 v[20:21], v[20:21], v[194:195]
	v_pk_mul_f32 v[18:19], v[18:19], v[192:193]
	v_pk_mul_f32 v[14:15], v[14:15], v[180:181]
	v_pk_mul_f32 v[10:11], v[10:11], v[184:185]
	v_pk_mul_f32 v[6:7], v[6:7], v[188:189]
	v_pk_mul_f32 v[16:17], v[16:17], v[182:183]
	v_pk_mul_f32 v[12:13], v[12:13], v[186:187]
	v_pk_mul_f32 v[8:9], v[8:9], v[190:191]
	v_pk_mul_f32 v[4:5], v[4:5], v[194:195]
	v_pk_mul_f32 v[2:3], v[2:3], v[192:193]
.LBB0_954:

	v_fmac_f32_e32 v81, v176, v96
	v_cvt_pk_bf16_f32 v176, v177, v178
	v_cvt_pk_bf16_f32 v177, v83, v84
	v_cvt_pk_bf16_f32 v178, v85, v86
	v_cvt_pk_bf16_f32 v179, v87, v179
	v_cvt_pk_bf16_f32 v84, v88, v89
	v_cvt_pk_bf16_f32 v85, v90, v91
	v_cvt_pk_bf16_f32 v86, v92, v93
	v_cvt_pk_bf16_f32 v87, v94, v95
	v_cvt_pk_bf16_f32 v66, v66, v67
	v_cvt_pk_bf16_f32 v67, v68, v69
	v_cvt_pk_bf16_f32 v68, v70, v71
	v_cvt_pk_bf16_f32 v69, v72, v82
	v_cvt_pk_bf16_f32 v70, v73, v74
	v_cvt_pk_bf16_f32 v71, v75, v76
	v_cvt_pk_bf16_f32 v72, v77, v78
	v_cvt_pk_bf16_f32 v73, v79, v80
	v_lshl_add_u32 v78, s48, 14, v169
	ds_read_b64_tr_b16 v[74:75], v78 offset:0
	ds_read_b64_tr_b16 v[76:77], v78 offset:0x800
	ds_read_b64_tr_b16 v[88:89], v78 offset:0x1000
	ds_read_b64_tr_b16 v[90:91], v78 offset:0x1800
	ds_read_b64_tr_b16 v[92:93], v78 offset:0x2000
	ds_read_b64_tr_b16 v[94:95], v78 offset:0x2800
	ds_read_b64_tr_b16 v[180:181], v78 offset:0x3000
	ds_read_b64_tr_b16 v[182:183], v78 offset:0x3800
	ds_read_b64_tr_b16 v[184:185], v78 offset:0x200
	ds_read_b64_tr_b16 v[186:187], v78 offset:0xa00
	ds_read_b64_tr_b16 v[188:189], v78 offset:0x1200
	ds_read_b64_tr_b16 v[190:191], v78 offset:0x1a00
	ds_read_b64_tr_b16 v[192:193], v78 offset:0x2200
	ds_read_b64_tr_b16 v[194:195], v78 offset:0x2a00
	ds_read_b64_tr_b16 v[196:197], v78 offset:0x3200
	ds_read_b64_tr_b16 v[198:199], v78 offset:0x3a00
	s_waitcnt lgkmcnt(8)


	v_mfma_f32_32x32x16_bf16 v[50:65], v[176:179], v[74:77], v[50:65]
	ds_read_b64_tr_b16 v[74:75], v78 offset:0x400
	ds_read_b64_tr_b16 v[76:77], v78 offset:0xc00
	v_mfma_f32_32x32x16_bf16 v[50:65], v[84:87], v[88:91], v[50:65]
	ds_read_b64_tr_b16 v[88:89], v78 offset:0x1400
	ds_read_b64_tr_b16 v[90:91], v78 offset:0x1c00
	v_mfma_f32_32x32x16_bf16 v[50:65], v[66:69], v[92:95], v[50:65]
	ds_read_b64_tr_b16 v[92:93], v78 offset:0x2400
	ds_read_b64_tr_b16 v[94:95], v78 offset:0x2c00
	ds_read_b64_tr_b16 v[200:201], v78 offset:0x3400
	ds_read_b64_tr_b16 v[202:203], v78 offset:0x3c00
	s_waitcnt lgkmcnt(8)
	v_mfma_f32_32x32x16_bf16 v[50:65], v[70:73], v[180:183], v[50:65]
	v_mfma_f32_32x32x16_bf16 v[34:49], v[176:179], v[184:187], v[34:49]
	ds_read_b64_tr_b16 v[180:181], v78 offset:0x600
	ds_read_b64_tr_b16 v[182:183], v78 offset:0xe00
	ds_read_b64_tr_b16 v[184:185], v78 offset:0x1600
	ds_read_b64_tr_b16 v[186:187], v78 offset:0x1e00
	v_mfma_f32_32x32x16_bf16 v[34:49], v[84:87], v[188:191], v[34:49]
	ds_read_b64_tr_b16 v[188:189], v78 offset:0x2600
	ds_read_b64_tr_b16 v[190:191], v78 offset:0x2e00
	v_mfma_f32_32x32x16_bf16 v[34:49], v[66:69], v[192:195], v[34:49]
	ds_read_b64_tr_b16 v[192:193], v78 offset:0x3600
	ds_read_b64_tr_b16 v[194:195], v78 offset:0x3e00
	s_waitcnt lgkmcnt(8)
	v_mfma_f32_32x32x16_bf16 v[34:49], v[70:73], v[196:199], v[34:49]
	v_mfma_f32_32x32x16_bf16 v[18:33], v[176:179], v[74:77], v[18:33]
	s_waitcnt lgkmcnt(0)
	v_mfma_f32_32x32x16_bf16 v[18:33], v[84:87], v[88:91], v[18:33]
	v_mfma_f32_32x32x16_bf16 v[18:33], v[66:69], v[92:95], v[18:33]
	v_mfma_f32_32x32x16_bf16 v[18:33], v[70:73], v[200:203], v[18:33]
	v_mfma_f32_32x32x16_bf16 v[2:17], v[176:179], v[180:183], v[2:17]
	s_add_i32 s47, s47, 64
	s_add_i32 s12, s12, 1
	s_add_u32 s94, s94, s16
	s_addc_u32 s95, s95, s17
	s_add_u32 s96, s96, s14
	s_addc_u32 s97, s97, s15


	v_mfma_f32_32x32x16_bf16 v[2:17], v[84:87], v[184:187], v[2:17]
	v_subrev_u32_e32 v167, 64, v167
	s_cmp_eq_u32 s54, s47
	v_mfma_f32_32x32x16_bf16 v[2:17], v[66:69], v[188:191], v[2:17]
	v_mfma_f32_32x32x16_bf16 v[2:17], v[70:73], v[192:195], v[2:17]
	s_cbranch_scc1 .LBB0_956
	v_mov_b32_e32 v176, v81
	s_add_i32 s44, s47, 0xe0
	s_cmp_ge_i32 s44, s55
	s_cbranch_scc0 .LBB0_946

.Lsm2_slow:
	v_mov_b32_e32 v178, v177
	s_nop 1
	v_permlane32_swap_b32_e32 v177, v178
	v_max_f32_e32 v177, v177, v178
	v_max_f32_e32 v177, 0, v177
	v_sub_f32_e32 v66, v66, v177
	v_sub_f32_e32 v67, v67, v177
	v_sub_f32_e32 v68, v68, v177
	v_sub_f32_e32 v69, v69, v177
	v_sub_f32_e32 v70, v70, v177
	v_sub_f32_e32 v71, v71, v177
	v_sub_f32_e32 v72, v72, v177
	v_sub_f32_e32 v73, v73, v177
	v_sub_f32_e32 v74, v74, v177
	v_sub_f32_e32 v75, v75, v177
	v_sub_f32_e32 v76, v76, v177
	v_sub_f32_e32 v77, v77, v177
	v_sub_f32_e32 v78, v78, v177
	v_sub_f32_e32 v79, v79, v177
	v_sub_f32_e32 v80, v80, v177
	v_sub_f32_e32 v81, v81, v177
	v_sub_f32_e32 v82, v82, v177
	v_sub_f32_e32 v83, v83, v177
	v_sub_f32_e32 v84, v84, v177
	v_sub_f32_e32 v85, v85, v177
	v_sub_f32_e32 v86, v86, v177
	v_sub_f32_e32 v87, v87, v177
	v_sub_f32_e32 v88, v88, v177
	v_sub_f32_e32 v89, v89, v177
	v_sub_f32_e32 v90, v90, v177
	v_sub_f32_e32 v91, v91, v177
	v_sub_f32_e32 v92, v92, v177
	v_sub_f32_e32 v93, v93, v177
	v_sub_f32_e32 v94, v94, v177
	v_sub_f32_e32 v95, v95, v177
	v_sub_f32_e32 v96, v96, v177
	v_sub_f32_e32 v97, v97, v177
	v_exp_f32_e64 v226, -v177
	v_add_f32_e32 v175, v175, v177
	v_sub_f32_e32 v210, 0, v175
	v_mov_b32_e32 v211, v210
	v_mov_b32_e32 v212, v210
	v_mov_b32_e32 v213, v210
	v_mov_b32_e32 v214, v210
	v_mov_b32_e32 v215, v210
	v_mov_b32_e32 v216, v210
	v_mov_b32_e32 v217, v210
	v_mov_b32_e32 v218, v210
	v_mov_b32_e32 v219, v210
	v_mov_b32_e32 v220, v210
	v_mov_b32_e32 v221, v210
	v_mov_b32_e32 v222, v210
	v_mov_b32_e32 v223, v210
	v_mov_b32_e32 v224, v210
	v_mov_b32_e32 v225, v210
	s_branch .Lsm2_join
.LBB0_956:
	v_mov_b32_e32 v97, v81
	s_nop 1
	v_permlane32_swap_b32_e32 v81, v97
	v_add_f32_e32 v81, v81, v97
	s_and_saveexec_b64 s[44:45], s[0:1]
	s_cbranch_execz .LBB0_958
	v_div_scale_f32 v66, s[0:1], v81, v81, 1.0
	v_rcp_f32_e32 v67, v66
	v_div_scale_f32 v68, vcc, 1.0, v81, 1.0
	v_fma_f32 v69, -v66, v67, 1.0
	v_fmac_f32_e32 v67, v69, v67
	v_mul_f32_e32 v69, v68, v67
	v_fma_f32 v70, -v66, v69, v68
	v_fmac_f32_e32 v69, v70, v67
	v_fma_f32 v66, -v66, v69, v68
	v_div_fmas_f32 v66, v66, v67, v69
	v_div_fixup_f32 v66, v66, v81, 1.0
	ds_write_b32 v168, v66 offset:128
